# v32: v25 + final combine: non-temporal policy on the once-read expert rows / x2 rows and the once-written output
# baseline (speedup 1.0000x reference)
; __device__ __forceinline__ void p12_final(const Frame& F, const KArgs& a) {
;     ...
;     for (int row = F.gw; row < NTOK; row += F.NGW) {
;         size_t so[4];
; #pragma unroll
;         for (int k = 0; k < 4; ++k) { const int e = TOPE[row * 4 + k], r = TOPR[row * 4 + k]; so[k] = (size_t)(tab[e] * 256 + r) * DM; }
;         f32x4 v[8]; float q = 0.f;
; #pragma unroll
;         for (int j = 0; j < 8; ++j) { const int c = 4 * (lane + 64 * j); { const u32x2 xr = *(const u32x2*)(X2 + (size_t)row * DM + c); v[j] = (f32x4){__builtin_bit_cast(float, xr.x << 16), __builtin_bit_cast(float, xr.x & 0xffff0000u), __builtin_bit_cast(float, xr.y << 16), __builtin_bit_cast(float, xr.y & 0xffff0000u)}; }
; #pragma unroll
;             for (int k = 0; k < 4; ++k) { const int y = *(const int*)(YB + so[k] + c);
;                 v[j][0] += __builtin_amdgcn_cvt_f32_fp8(y, 0); v[j][1] += __builtin_amdgcn_cvt_f32_fp8(y, 1); v[j][2] += __builtin_amdgcn_cvt_f32_fp8(y, 2); v[j][3] += __builtin_amdgcn_cvt_f32_fp8(y, 3); }
;             q += (v[j][0] * v[j][0] + v[j][1] * v[j][1]) + (v[j][2] * v[j][2] + v[j][3] * v[j][3]); }
.Lp12_row:
	s_lshl_b32 s12, s20, 13
	s_add_u32 s18, s6, s12
	s_addc_u32 s19, s7, 0
	s_add_u32 s24, s18, 0x1000
	s_addc_u32 s25, s19, 0
	s_add_i32 s21, s20, s94
	s_waitcnt vmcnt(13)
	v_lshlrev_b32_e32 v8, 2, v8
	v_lshlrev_b32_e32 v9, 2, v9
	v_lshlrev_b32_e32 v10, 2, v10
	v_lshlrev_b32_e32 v11, 2, v11
	v_add_u32_e32 v8, 0x20100, v8
	v_add_u32_e32 v9, 0x20100, v9
	v_add_u32_e32 v10, 0x20100, v10
	v_add_u32_e32 v11, 0x20100, v11
	ds_read_b32 v8, v8
	ds_read_b32 v9, v9
	ds_read_b32 v10, v10
	ds_read_b32 v11, v11
	s_waitcnt vmcnt(12) lgkmcnt(0)
	v_lshl_add_u32 v8, v8, 8, v12
	v_lshl_add_u32 v9, v9, 8, v13
	v_lshl_add_u32 v10, v10, 8, v14
	v_lshl_add_u32 v11, v11, 8, v15
	v_lshl_add_u32 v8, v8, 11, v2
	v_lshl_add_u32 v9, v9, 11, v2
	v_lshl_add_u32 v10, v10, 11, v2
	v_lshl_add_u32 v11, v11, 11, v2
	global_load_dwordx2 v[32:33], v8, s[0:1] nt
	global_load_dwordx2 v[40:41], v9, s[0:1] nt
	global_load_dwordx2 v[48:49], v10, s[0:1] nt
	global_load_dwordx2 v[56:57], v11, s[0:1] nt
	global_load_dwordx2 v[34:35], v8, s[0:1] offset:512 nt
	global_load_dwordx2 v[42:43], v9, s[0:1] offset:512 nt
	global_load_dwordx2 v[50:51], v10, s[0:1] offset:512 nt
	global_load_dwordx2 v[58:59], v11, s[0:1] offset:512 nt
	global_load_dwordx2 v[36:37], v8, s[0:1] offset:1024 nt
	global_load_dwordx2 v[44:45], v9, s[0:1] offset:1024 nt
	global_load_dwordx2 v[52:53], v10, s[0:1] offset:1024 nt
	global_load_dwordx2 v[60:61], v11, s[0:1] offset:1024 nt
	global_load_dwordx2 v[38:39], v8, s[0:1] offset:1536 nt
	global_load_dwordx2 v[46:47], v9, s[0:1] offset:1536 nt
	global_load_dwordx2 v[54:55], v10, s[0:1] offset:1536 nt
	global_load_dwordx2 v[62:63], v11, s[0:1] offset:1536 nt
	s_lshl_b32 s12, s21, 4
	s_add_u32 s14, s8, s12
	s_addc_u32 s15, s9, 0
	s_add_u32 s16, s10, s12
	s_addc_u32 s17, s11, 0
	global_load_dwordx4 v[110:113], v5, s[14:15]
	global_load_dwordx4 v[114:117], v5, s[16:17]
	s_lshl_b32 s12, s21, 12
	s_add_u32 s14, s2, s12
	s_addc_u32 s15, s3, 0
	global_load_dwordx4 v[118:121], v3, s[14:15] nt
	global_load_dwordx4 v[122:125], v3, s[14:15] offset:1024 nt
	global_load_dwordx4 v[126:129], v3, s[14:15] offset:2048 nt
	global_load_dwordx4 v[130:133], v3, s[14:15] offset:3072 nt
	s_waitcnt vmcnt(30)
	v_lshlrev_b32_e32 v64, 16, v16
	v_and_b32_e32 v65, 0xffff0000, v16
	v_lshlrev_b32_e32 v66, 16, v17
	v_and_b32_e32 v67, 0xffff0000, v17
	v_lshlrev_b32_e32 v68, 16, v18
	v_and_b32_e32 v69, 0xffff0000, v18
	v_lshlrev_b32_e32 v70, 16, v19
	v_and_b32_e32 v71, 0xffff0000, v19
	v_lshlrev_b32_e32 v72, 16, v20
	v_and_b32_e32 v73, 0xffff0000, v20
	v_lshlrev_b32_e32 v74, 16, v21
	v_and_b32_e32 v75, 0xffff0000, v21
	v_lshlrev_b32_e32 v76, 16, v22
	v_and_b32_e32 v77, 0xffff0000, v22
	v_lshlrev_b32_e32 v78, 16, v23
	v_and_b32_e32 v79, 0xffff0000, v23
	v_lshlrev_b32_e32 v80, 16, v24
	v_and_b32_e32 v81, 0xffff0000, v24
	v_lshlrev_b32_e32 v82, 16, v25
	v_and_b32_e32 v83, 0xffff0000, v25
	v_lshlrev_b32_e32 v84, 16, v26
	v_and_b32_e32 v85, 0xffff0000, v26
	v_lshlrev_b32_e32 v86, 16, v27
	v_and_b32_e32 v87, 0xffff0000, v27
	v_lshlrev_b32_e32 v88, 16, v28
	v_and_b32_e32 v89, 0xffff0000, v28
	v_lshlrev_b32_e32 v90, 16, v29
	v_and_b32_e32 v91, 0xffff0000, v29
	v_lshlrev_b32_e32 v92, 16, v30
	v_and_b32_e32 v93, 0xffff0000, v30
	v_lshlrev_b32_e32 v94, 16, v31
	v_and_b32_e32 v95, 0xffff0000, v31
	s_waitcnt vmcnt(18)
	v_cvt_f32_fp8_e32 v96, v32
	v_cvt_f32_fp8_sdwa v97, v32 src0_sel:BYTE_1
	v_cvt_f32_fp8_sdwa v98, v32 src0_sel:BYTE_2
	v_cvt_f32_fp8_sdwa v99, v32 src0_sel:BYTE_3
	v_cvt_f32_fp8_e32 v100, v33
	v_cvt_f32_fp8_sdwa v101, v33 src0_sel:BYTE_1
	v_cvt_f32_fp8_sdwa v102, v33 src0_sel:BYTE_2
	v_cvt_f32_fp8_sdwa v103, v33 src0_sel:BYTE_3
	v_pk_add_f32 v[64:65], v[64:65], v[96:97]
	v_pk_add_f32 v[66:67], v[66:67], v[98:99]
	v_pk_add_f32 v[68:69], v[68:69], v[100:101]
	v_pk_add_f32 v[70:71], v[70:71], v[102:103]
	v_cvt_f32_fp8_e32 v96, v40
	v_cvt_f32_fp8_sdwa v97, v40 src0_sel:BYTE_1
	v_cvt_f32_fp8_sdwa v98, v40 src0_sel:BYTE_2
	v_cvt_f32_fp8_sdwa v99, v40 src0_sel:BYTE_3
	v_cvt_f32_fp8_e32 v100, v41
	v_cvt_f32_fp8_sdwa v101, v41 src0_sel:BYTE_1
	v_cvt_f32_fp8_sdwa v102, v41 src0_sel:BYTE_2
	v_cvt_f32_fp8_sdwa v103, v41 src0_sel:BYTE_3
	v_pk_add_f32 v[64:65], v[64:65], v[96:97]
	v_pk_add_f32 v[66:67], v[66:67], v[98:99]
	v_pk_add_f32 v[68:69], v[68:69], v[100:101]
	v_pk_add_f32 v[70:71], v[70:71], v[102:103]
	v_cvt_f32_fp8_e32 v96, v48
	v_cvt_f32_fp8_sdwa v97, v48 src0_sel:BYTE_1
	v_cvt_f32_fp8_sdwa v98, v48 src0_sel:BYTE_2
	v_cvt_f32_fp8_sdwa v99, v48 src0_sel:BYTE_3
	v_cvt_f32_fp8_e32 v100, v49
	v_cvt_f32_fp8_sdwa v101, v49 src0_sel:BYTE_1
	v_cvt_f32_fp8_sdwa v102, v49 src0_sel:BYTE_2
	v_cvt_f32_fp8_sdwa v103, v49 src0_sel:BYTE_3
	v_pk_add_f32 v[64:65], v[64:65], v[96:97]
	v_pk_add_f32 v[66:67], v[66:67], v[98:99]
	v_pk_add_f32 v[68:69], v[68:69], v[100:101]
	v_pk_add_f32 v[70:71], v[70:71], v[102:103]
	v_cvt_f32_fp8_e32 v96, v56
	v_cvt_f32_fp8_sdwa v97, v56 src0_sel:BYTE_1
	v_cvt_f32_fp8_sdwa v98, v56 src0_sel:BYTE_2
	v_cvt_f32_fp8_sdwa v99, v56 src0_sel:BYTE_3
	v_cvt_f32_fp8_e32 v100, v57
	v_cvt_f32_fp8_sdwa v101, v57 src0_sel:BYTE_1
	v_cvt_f32_fp8_sdwa v102, v57 src0_sel:BYTE_2
	v_cvt_f32_fp8_sdwa v103, v57 src0_sel:BYTE_3
	v_pk_add_f32 v[64:65], v[64:65], v[96:97]
	v_pk_add_f32 v[66:67], v[66:67], v[98:99]
	v_pk_add_f32 v[68:69], v[68:69], v[100:101]
	v_pk_add_f32 v[70:71], v[70:71], v[102:103]
	s_waitcnt vmcnt(14)
; __device__ __forceinline__ void p12_final(const Frame& F, const KArgs& a) {
;     ...
;         for (int j = 0; j < 8; ++j) { const int c = 4 * (lane + 64 * j); { const u32x2 xr = *(const u32x2*)(X2 + (size_t)row * DM + c); v[j] = (f32x4){__builtin_bit_cast(float, xr.x << 16), __builtin_bit_cast(float, xr.x & 0xffff0000u), __builtin_bit_cast(float, xr.y << 16), __builtin_bit_cast(float, xr.y & 0xffff0000u)}; }
; #pragma unroll
;             for (int k = 0; k < 4; ++k) { const int y = *(const int*)(YB + so[k] + c);
;                 v[j][0] += __builtin_amdgcn_cvt_f32_fp8(y, 0); v[j][1] += __builtin_amdgcn_cvt_f32_fp8(y, 1); v[j][2] += __builtin_amdgcn_cvt_f32_fp8(y, 2); v[j][3] += __builtin_amdgcn_cvt_f32_fp8(y, 3); }
;             q += (v[j][0] * v[j][0] + v[j][1] * v[j][1]) + (v[j][2] * v[j][2] + v[j][3] * v[j][3]); }
	v_cvt_f32_fp8_e32 v96, v34
	v_cvt_f32_fp8_sdwa v97, v34 src0_sel:BYTE_1
	v_cvt_f32_fp8_sdwa v98, v34 src0_sel:BYTE_2
	v_cvt_f32_fp8_sdwa v99, v34 src0_sel:BYTE_3
	v_cvt_f32_fp8_e32 v100, v35
	v_cvt_f32_fp8_sdwa v101, v35 src0_sel:BYTE_1
	v_cvt_f32_fp8_sdwa v102, v35 src0_sel:BYTE_2
	v_cvt_f32_fp8_sdwa v103, v35 src0_sel:BYTE_3
	v_pk_add_f32 v[72:73], v[72:73], v[96:97]
	v_pk_add_f32 v[74:75], v[74:75], v[98:99]
	v_pk_add_f32 v[76:77], v[76:77], v[100:101]
	v_pk_add_f32 v[78:79], v[78:79], v[102:103]
	v_cvt_f32_fp8_e32 v96, v42
	v_cvt_f32_fp8_sdwa v97, v42 src0_sel:BYTE_1
	v_cvt_f32_fp8_sdwa v98, v42 src0_sel:BYTE_2
	v_cvt_f32_fp8_sdwa v99, v42 src0_sel:BYTE_3
	v_cvt_f32_fp8_e32 v100, v43
	v_cvt_f32_fp8_sdwa v101, v43 src0_sel:BYTE_1
	v_cvt_f32_fp8_sdwa v102, v43 src0_sel:BYTE_2
	v_cvt_f32_fp8_sdwa v103, v43 src0_sel:BYTE_3
	v_pk_add_f32 v[72:73], v[72:73], v[96:97]
	v_pk_add_f32 v[74:75], v[74:75], v[98:99]
	v_pk_add_f32 v[76:77], v[76:77], v[100:101]
	v_pk_add_f32 v[78:79], v[78:79], v[102:103]
	v_cvt_f32_fp8_e32 v96, v50
	v_cvt_f32_fp8_sdwa v97, v50 src0_sel:BYTE_1
	v_cvt_f32_fp8_sdwa v98, v50 src0_sel:BYTE_2
	v_cvt_f32_fp8_sdwa v99, v50 src0_sel:BYTE_3
	v_cvt_f32_fp8_e32 v100, v51
	v_cvt_f32_fp8_sdwa v101, v51 src0_sel:BYTE_1
	v_cvt_f32_fp8_sdwa v102, v51 src0_sel:BYTE_2
	v_cvt_f32_fp8_sdwa v103, v51 src0_sel:BYTE_3
	v_pk_add_f32 v[72:73], v[72:73], v[96:97]
	v_pk_add_f32 v[74:75], v[74:75], v[98:99]
	v_pk_add_f32 v[76:77], v[76:77], v[100:101]
	v_pk_add_f32 v[78:79], v[78:79], v[102:103]
	v_cvt_f32_fp8_e32 v96, v58
	v_cvt_f32_fp8_sdwa v97, v58 src0_sel:BYTE_1
	v_cvt_f32_fp8_sdwa v98, v58 src0_sel:BYTE_2
	v_cvt_f32_fp8_sdwa v99, v58 src0_sel:BYTE_3
	v_cvt_f32_fp8_e32 v100, v59
	v_cvt_f32_fp8_sdwa v101, v59 src0_sel:BYTE_1
	v_cvt_f32_fp8_sdwa v102, v59 src0_sel:BYTE_2
	v_cvt_f32_fp8_sdwa v103, v59 src0_sel:BYTE_3
	v_pk_add_f32 v[72:73], v[72:73], v[96:97]
	v_pk_add_f32 v[74:75], v[74:75], v[98:99]
	v_pk_add_f32 v[76:77], v[76:77], v[100:101]
	v_pk_add_f32 v[78:79], v[78:79], v[102:103]
	s_waitcnt vmcnt(10)
	v_cvt_f32_fp8_e32 v96, v36
	v_cvt_f32_fp8_sdwa v97, v36 src0_sel:BYTE_1
	v_cvt_f32_fp8_sdwa v98, v36 src0_sel:BYTE_2
	v_cvt_f32_fp8_sdwa v99, v36 src0_sel:BYTE_3
	v_cvt_f32_fp8_e32 v100, v37
	v_cvt_f32_fp8_sdwa v101, v37 src0_sel:BYTE_1
	v_cvt_f32_fp8_sdwa v102, v37 src0_sel:BYTE_2
	v_cvt_f32_fp8_sdwa v103, v37 src0_sel:BYTE_3
	v_pk_add_f32 v[80:81], v[80:81], v[96:97]
	v_pk_add_f32 v[82:83], v[82:83], v[98:99]
	v_pk_add_f32 v[84:85], v[84:85], v[100:101]
	v_pk_add_f32 v[86:87], v[86:87], v[102:103]
	v_cvt_f32_fp8_e32 v96, v44
	v_cvt_f32_fp8_sdwa v97, v44 src0_sel:BYTE_1
	v_cvt_f32_fp8_sdwa v98, v44 src0_sel:BYTE_2
	v_cvt_f32_fp8_sdwa v99, v44 src0_sel:BYTE_3
	v_cvt_f32_fp8_e32 v100, v45
	v_cvt_f32_fp8_sdwa v101, v45 src0_sel:BYTE_1
	v_cvt_f32_fp8_sdwa v102, v45 src0_sel:BYTE_2
	v_cvt_f32_fp8_sdwa v103, v45 src0_sel:BYTE_3
	v_pk_add_f32 v[80:81], v[80:81], v[96:97]
	v_pk_add_f32 v[82:83], v[82:83], v[98:99]
	v_pk_add_f32 v[84:85], v[84:85], v[100:101]
	v_pk_add_f32 v[86:87], v[86:87], v[102:103]
	v_cvt_f32_fp8_e32 v96, v52
	v_cvt_f32_fp8_sdwa v97, v52 src0_sel:BYTE_1
	v_cvt_f32_fp8_sdwa v98, v52 src0_sel:BYTE_2
	v_cvt_f32_fp8_sdwa v99, v52 src0_sel:BYTE_3
	v_cvt_f32_fp8_e32 v100, v53
	v_cvt_f32_fp8_sdwa v101, v53 src0_sel:BYTE_1
	v_cvt_f32_fp8_sdwa v102, v53 src0_sel:BYTE_2
	v_cvt_f32_fp8_sdwa v103, v53 src0_sel:BYTE_3
	v_pk_add_f32 v[80:81], v[80:81], v[96:97]
	v_pk_add_f32 v[82:83], v[82:83], v[98:99]
	v_pk_add_f32 v[84:85], v[84:85], v[100:101]
	v_pk_add_f32 v[86:87], v[86:87], v[102:103]
	v_cvt_f32_fp8_e32 v96, v60
	v_cvt_f32_fp8_sdwa v97, v60 src0_sel:BYTE_1
	v_cvt_f32_fp8_sdwa v98, v60 src0_sel:BYTE_2
	v_cvt_f32_fp8_sdwa v99, v60 src0_sel:BYTE_3
	v_cvt_f32_fp8_e32 v100, v61
	v_cvt_f32_fp8_sdwa v101, v61 src0_sel:BYTE_1
	v_cvt_f32_fp8_sdwa v102, v61 src0_sel:BYTE_2
	v_cvt_f32_fp8_sdwa v103, v61 src0_sel:BYTE_3
	v_pk_add_f32 v[80:81], v[80:81], v[96:97]
	v_pk_add_f32 v[82:83], v[82:83], v[98:99]
	v_pk_add_f32 v[84:85], v[84:85], v[100:101]
	v_pk_add_f32 v[86:87], v[86:87], v[102:103]
	s_waitcnt vmcnt(6)
	v_cvt_f32_fp8_e32 v96, v38
	v_cvt_f32_fp8_sdwa v97, v38 src0_sel:BYTE_1
	v_cvt_f32_fp8_sdwa v98, v38 src0_sel:BYTE_2
	v_cvt_f32_fp8_sdwa v99, v38 src0_sel:BYTE_3
	v_cvt_f32_fp8_e32 v100, v39
	v_cvt_f32_fp8_sdwa v101, v39 src0_sel:BYTE_1
	v_cvt_f32_fp8_sdwa v102, v39 src0_sel:BYTE_2
	v_cvt_f32_fp8_sdwa v103, v39 src0_sel:BYTE_3
	v_pk_add_f32 v[88:89], v[88:89], v[96:97]
	v_pk_add_f32 v[90:91], v[90:91], v[98:99]
	v_pk_add_f32 v[92:93], v[92:93], v[100:101]
	v_pk_add_f32 v[94:95], v[94:95], v[102:103]
	v_cvt_f32_fp8_e32 v96, v46
	v_cvt_f32_fp8_sdwa v97, v46 src0_sel:BYTE_1
	v_cvt_f32_fp8_sdwa v98, v46 src0_sel:BYTE_2
	v_cvt_f32_fp8_sdwa v99, v46 src0_sel:BYTE_3
	v_cvt_f32_fp8_e32 v100, v47
	v_cvt_f32_fp8_sdwa v101, v47 src0_sel:BYTE_1
	v_cvt_f32_fp8_sdwa v102, v47 src0_sel:BYTE_2
	v_cvt_f32_fp8_sdwa v103, v47 src0_sel:BYTE_3
	v_pk_add_f32 v[88:89], v[88:89], v[96:97]
	v_pk_add_f32 v[90:91], v[90:91], v[98:99]
	v_pk_add_f32 v[92:93], v[92:93], v[100:101]
	v_pk_add_f32 v[94:95], v[94:95], v[102:103]
	v_cvt_f32_fp8_e32 v96, v54
	v_cvt_f32_fp8_sdwa v97, v54 src0_sel:BYTE_1
	v_cvt_f32_fp8_sdwa v98, v54 src0_sel:BYTE_2
	v_cvt_f32_fp8_sdwa v99, v54 src0_sel:BYTE_3
	v_cvt_f32_fp8_e32 v100, v55
	v_cvt_f32_fp8_sdwa v101, v55 src0_sel:BYTE_1
	v_cvt_f32_fp8_sdwa v102, v55 src0_sel:BYTE_2
	v_cvt_f32_fp8_sdwa v103, v55 src0_sel:BYTE_3
	v_pk_add_f32 v[88:89], v[88:89], v[96:97]
	v_pk_add_f32 v[90:91], v[90:91], v[98:99]
	v_pk_add_f32 v[92:93], v[92:93], v[100:101]
	v_pk_add_f32 v[94:95], v[94:95], v[102:103]
	v_cvt_f32_fp8_e32 v96, v62
; __device__ __forceinline__ void p12_final(const Frame& F, const KArgs& a) {
;     ...
;         for (int j = 0; j < 8; ++j) { const int c = 4 * (lane + 64 * j); { const u32x2 xr = *(const u32x2*)(X2 + (size_t)row * DM + c); v[j] = (f32x4){__builtin_bit_cast(float, xr.x << 16), __builtin_bit_cast(float, xr.x & 0xffff0000u), __builtin_bit_cast(float, xr.y << 16), __builtin_bit_cast(float, xr.y & 0xffff0000u)}; }
; #pragma unroll
;             for (int k = 0; k < 4; ++k) { const int y = *(const int*)(YB + so[k] + c);
;                 v[j][0] += __builtin_amdgcn_cvt_f32_fp8(y, 0); v[j][1] += __builtin_amdgcn_cvt_f32_fp8(y, 1); v[j][2] += __builtin_amdgcn_cvt_f32_fp8(y, 2); v[j][3] += __builtin_amdgcn_cvt_f32_fp8(y, 3); }
;             q += (v[j][0] * v[j][0] + v[j][1] * v[j][1]) + (v[j][2] * v[j][2] + v[j][3] * v[j][3]); }
;         const float rs = rsqrtf(wave_sum(q) * (1.f / DM) + RMS_EPS);
; #pragma unroll
;         for (int j = 0; j < 8; ++j) { const int c = 4 * (lane + 64 * j); const f32x4 g = *(const f32x4*)(a.in[24] + c); *(f32x4*)(a.out + (size_t)row * DM + c) = v[j] * rs * g; }
	v_cvt_f32_fp8_sdwa v97, v62 src0_sel:BYTE_1
	v_cvt_f32_fp8_sdwa v98, v62 src0_sel:BYTE_2
	v_cvt_f32_fp8_sdwa v99, v62 src0_sel:BYTE_3
	v_cvt_f32_fp8_e32 v100, v63
	v_cvt_f32_fp8_sdwa v101, v63 src0_sel:BYTE_1
	v_cvt_f32_fp8_sdwa v102, v63 src0_sel:BYTE_2
	v_cvt_f32_fp8_sdwa v103, v63 src0_sel:BYTE_3
	v_pk_add_f32 v[88:89], v[88:89], v[96:97]
	v_pk_add_f32 v[90:91], v[90:91], v[98:99]
	v_pk_add_f32 v[92:93], v[92:93], v[100:101]
	v_pk_add_f32 v[94:95], v[94:95], v[102:103]
	v_pk_mul_f32 v[106:107], v[64:65], v[64:65]
	v_pk_fma_f32 v[106:107], v[66:67], v[66:67], v[106:107]
	v_pk_fma_f32 v[106:107], v[68:69], v[68:69], v[106:107]
	v_pk_fma_f32 v[106:107], v[70:71], v[70:71], v[106:107]
	v_pk_fma_f32 v[106:107], v[72:73], v[72:73], v[106:107]
	v_pk_fma_f32 v[106:107], v[74:75], v[74:75], v[106:107]
	v_pk_fma_f32 v[106:107], v[76:77], v[76:77], v[106:107]
	v_pk_fma_f32 v[106:107], v[78:79], v[78:79], v[106:107]
	v_pk_fma_f32 v[106:107], v[80:81], v[80:81], v[106:107]
	v_pk_fma_f32 v[106:107], v[82:83], v[82:83], v[106:107]
	v_pk_fma_f32 v[106:107], v[84:85], v[84:85], v[106:107]
	v_pk_fma_f32 v[106:107], v[86:87], v[86:87], v[106:107]
	v_pk_fma_f32 v[106:107], v[88:89], v[88:89], v[106:107]
	v_pk_fma_f32 v[106:107], v[90:91], v[90:91], v[106:107]
	v_pk_fma_f32 v[106:107], v[92:93], v[92:93], v[106:107]
	v_pk_fma_f32 v[106:107], v[94:95], v[94:95], v[106:107]
	s_nop 0
	v_add_f32_e32 v105, v106, v107
	s_nop 1
	v_add_f32_dpp v105, v105, v105 quad_perm:[1,0,3,2] row_mask:0xf bank_mask:0xf
	s_nop 1
	v_add_f32_dpp v105, v105, v105 quad_perm:[2,3,0,1] row_mask:0xf bank_mask:0xf
	s_nop 1
	v_add_f32_dpp v105, v105, v105 row_half_mirror row_mask:0xf bank_mask:0xf
	s_nop 1
	v_add_f32_dpp v105, v105, v105 row_mirror row_mask:0xf bank_mask:0xf
	s_nop 1
	v_readlane_b32 s12, v105, 0
	v_readlane_b32 s14, v105, 16
	v_readlane_b32 s15, v105, 32
	v_readlane_b32 s16, v105, 48
	s_nop 1
	v_mov_b32_e32 v105, s12
	v_add_f32_e32 v105, s14, v105
	v_add_f32_e32 v105, s15, v105
	v_add_f32_e32 v105, s16, v105
	v_fmamk_f32 v105, v105, 0x3a000000, v104
	v_rsq_f32_e32 v108, v105
	s_nop 0
	v_pk_mul_f32 v[64:65], v[64:65], v[108:109] op_sel_hi:[1,0]
	v_pk_mul_f32 v[66:67], v[66:67], v[108:109] op_sel_hi:[1,0]
	v_pk_mul_f32 v[68:69], v[68:69], v[108:109] op_sel_hi:[1,0]
	v_pk_mul_f32 v[70:71], v[70:71], v[108:109] op_sel_hi:[1,0]
	v_pk_mul_f32 v[64:65], v[64:65], v[200:201]
	v_pk_mul_f32 v[66:67], v[66:67], v[202:203]
	v_pk_mul_f32 v[68:69], v[68:69], v[204:205]
	v_pk_mul_f32 v[70:71], v[70:71], v[206:207]
	global_store_dwordx4 v4, v[64:67], s[18:19] nt
	global_store_dwordx4 v4, v[68:71], s[18:19] offset:16 nt
	v_pk_mul_f32 v[72:73], v[72:73], v[108:109] op_sel_hi:[1,0]
	v_pk_mul_f32 v[74:75], v[74:75], v[108:109] op_sel_hi:[1,0]
	v_pk_mul_f32 v[76:77], v[76:77], v[108:109] op_sel_hi:[1,0]
	v_pk_mul_f32 v[78:79], v[78:79], v[108:109] op_sel_hi:[1,0]
	v_pk_mul_f32 v[72:73], v[72:73], v[208:209]
	v_pk_mul_f32 v[74:75], v[74:75], v[210:211]
	v_pk_mul_f32 v[76:77], v[76:77], v[212:213]
	v_pk_mul_f32 v[78:79], v[78:79], v[214:215]
	global_store_dwordx4 v4, v[72:75], s[18:19] offset:2048 nt
	global_store_dwordx4 v4, v[76:79], s[18:19] offset:2064 nt
	v_pk_mul_f32 v[80:81], v[80:81], v[108:109] op_sel_hi:[1,0]
	v_pk_mul_f32 v[82:83], v[82:83], v[108:109] op_sel_hi:[1,0]
	v_pk_mul_f32 v[84:85], v[84:85], v[108:109] op_sel_hi:[1,0]
	v_pk_mul_f32 v[86:87], v[86:87], v[108:109] op_sel_hi:[1,0]
	v_pk_mul_f32 v[80:81], v[80:81], v[216:217]
	v_pk_mul_f32 v[82:83], v[82:83], v[218:219]
	v_pk_mul_f32 v[84:85], v[84:85], v[220:221]
	v_pk_mul_f32 v[86:87], v[86:87], v[222:223]
	global_store_dwordx4 v4, v[80:83], s[24:25] nt
	global_store_dwordx4 v4, v[84:87], s[24:25] offset:16 nt
	v_pk_mul_f32 v[88:89], v[88:89], v[108:109] op_sel_hi:[1,0]
	v_pk_mul_f32 v[90:91], v[90:91], v[108:109] op_sel_hi:[1,0]
	v_pk_mul_f32 v[92:93], v[92:93], v[108:109] op_sel_hi:[1,0]
	v_pk_mul_f32 v[94:95], v[94:95], v[108:109] op_sel_hi:[1,0]
	v_pk_mul_f32 v[88:89], v[88:89], v[224:225]
	v_pk_mul_f32 v[90:91], v[90:91], v[226:227]
	v_pk_mul_f32 v[92:93], v[92:93], v[228:229]
	v_pk_mul_f32 v[94:95], v[94:95], v[230:231]
	global_store_dwordx4 v4, v[88:91], s[24:25] offset:2048 nt
	global_store_dwordx4 v4, v[92:95], s[24:25] offset:2064 nt
	s_mov_b32 s20, s21
	s_lshl_b32 s12, s20, 13
	s_add_u32 s18, s6, s12
	s_addc_u32 s19, s7, 0
	s_add_u32 s24, s18, 0x1000
	s_addc_u32 s25, s19, 0
	s_add_i32 s21, s20, s94
	s_waitcnt vmcnt(13)
	v_lshlrev_b32_e32 v110, 2, v110
	v_lshlrev_b32_e32 v111, 2, v111
	v_lshlrev_b32_e32 v112, 2, v112
	v_lshlrev_b32_e32 v113, 2, v113
	v_add_u32_e32 v110, 0x20100, v110
	v_add_u32_e32 v111, 0x20100, v111
	v_add_u32_e32 v112, 0x20100, v112
	v_add_u32_e32 v113, 0x20100, v113
	ds_read_b32 v110, v110
	ds_read_b32 v111, v111
	ds_read_b32 v112, v112
	ds_read_b32 v113, v113
	s_waitcnt vmcnt(12) lgkmcnt(0)
; __device__ __forceinline__ void p12_final(const Frame& F, const KArgs& a) {
;     ...
;         for (int k = 0; k < 4; ++k) { const int e = TOPE[row * 4 + k], r = TOPR[row * 4 + k]; so[k] = (size_t)(tab[e] * 256 + r) * DM; }
;         f32x4 v[8]; float q = 0.f;
; #pragma unroll
;         for (int j = 0; j < 8; ++j) { const int c = 4 * (lane + 64 * j); { const u32x2 xr = *(const u32x2*)(X2 + (size_t)row * DM + c); v[j] = (f32x4){__builtin_bit_cast(float, xr.x << 16), __builtin_bit_cast(float, xr.x & 0xffff0000u), __builtin_bit_cast(float, xr.y << 16), __builtin_bit_cast(float, xr.y & 0xffff0000u)}; }
; #pragma unroll
;             for (int k = 0; k < 4; ++k) { const int y = *(const int*)(YB + so[k] + c);
;                 v[j][0] += __builtin_amdgcn_cvt_f32_fp8(y, 0); v[j][1] += __builtin_amdgcn_cvt_f32_fp8(y, 1); v[j][2] += __builtin_amdgcn_cvt_f32_fp8(y, 2); v[j][3] += __builtin_amdgcn_cvt_f32_fp8(y, 3); }
	v_lshl_add_u32 v110, v110, 8, v114
	v_lshl_add_u32 v111, v111, 8, v115
	v_lshl_add_u32 v112, v112, 8, v116
	v_lshl_add_u32 v113, v113, 8, v117
	v_lshl_add_u32 v110, v110, 11, v2
	v_lshl_add_u32 v111, v111, 11, v2
	v_lshl_add_u32 v112, v112, 11, v2
	v_lshl_add_u32 v113, v113, 11, v2
	global_load_dwordx2 v[32:33], v110, s[0:1] nt
	global_load_dwordx2 v[40:41], v111, s[0:1] nt
	global_load_dwordx2 v[48:49], v112, s[0:1] nt
	global_load_dwordx2 v[56:57], v113, s[0:1] nt
	global_load_dwordx2 v[34:35], v110, s[0:1] offset:512 nt
	global_load_dwordx2 v[42:43], v111, s[0:1] offset:512 nt
	global_load_dwordx2 v[50:51], v112, s[0:1] offset:512 nt
	global_load_dwordx2 v[58:59], v113, s[0:1] offset:512 nt
	global_load_dwordx2 v[36:37], v110, s[0:1] offset:1024 nt
	global_load_dwordx2 v[44:45], v111, s[0:1] offset:1024 nt
	global_load_dwordx2 v[52:53], v112, s[0:1] offset:1024 nt
	global_load_dwordx2 v[60:61], v113, s[0:1] offset:1024 nt
	global_load_dwordx2 v[38:39], v110, s[0:1] offset:1536 nt
	global_load_dwordx2 v[46:47], v111, s[0:1] offset:1536 nt
	global_load_dwordx2 v[54:55], v112, s[0:1] offset:1536 nt
	global_load_dwordx2 v[62:63], v113, s[0:1] offset:1536 nt
	s_lshl_b32 s12, s21, 4
	s_add_u32 s14, s8, s12
	s_addc_u32 s15, s9, 0
	s_add_u32 s16, s10, s12
	s_addc_u32 s17, s11, 0
	global_load_dwordx4 v[8:11], v5, s[14:15]
	global_load_dwordx4 v[12:15], v5, s[16:17]
	s_lshl_b32 s12, s21, 12
	s_add_u32 s14, s2, s12
	s_addc_u32 s15, s3, 0
	global_load_dwordx4 v[16:19], v3, s[14:15] nt
	global_load_dwordx4 v[20:23], v3, s[14:15] offset:1024 nt
	global_load_dwordx4 v[24:27], v3, s[14:15] offset:2048 nt
	global_load_dwordx4 v[28:31], v3, s[14:15] offset:3072 nt
	s_waitcnt vmcnt(30)
	v_lshlrev_b32_e32 v64, 16, v118
	v_and_b32_e32 v65, 0xffff0000, v118
	v_lshlrev_b32_e32 v66, 16, v119
	v_and_b32_e32 v67, 0xffff0000, v119
	v_lshlrev_b32_e32 v68, 16, v120
	v_and_b32_e32 v69, 0xffff0000, v120
	v_lshlrev_b32_e32 v70, 16, v121
	v_and_b32_e32 v71, 0xffff0000, v121
	v_lshlrev_b32_e32 v72, 16, v122
	v_and_b32_e32 v73, 0xffff0000, v122
	v_lshlrev_b32_e32 v74, 16, v123
	v_and_b32_e32 v75, 0xffff0000, v123
	v_lshlrev_b32_e32 v76, 16, v124
	v_and_b32_e32 v77, 0xffff0000, v124
	v_lshlrev_b32_e32 v78, 16, v125
	v_and_b32_e32 v79, 0xffff0000, v125
	v_lshlrev_b32_e32 v80, 16, v126
	v_and_b32_e32 v81, 0xffff0000, v126
	v_lshlrev_b32_e32 v82, 16, v127
	v_and_b32_e32 v83, 0xffff0000, v127
	v_lshlrev_b32_e32 v84, 16, v128
	v_and_b32_e32 v85, 0xffff0000, v128
	v_lshlrev_b32_e32 v86, 16, v129
	v_and_b32_e32 v87, 0xffff0000, v129
	v_lshlrev_b32_e32 v88, 16, v130
	v_and_b32_e32 v89, 0xffff0000, v130
	v_lshlrev_b32_e32 v90, 16, v131
	v_and_b32_e32 v91, 0xffff0000, v131
	v_lshlrev_b32_e32 v92, 16, v132
	v_and_b32_e32 v93, 0xffff0000, v132
	v_lshlrev_b32_e32 v94, 16, v133
	v_and_b32_e32 v95, 0xffff0000, v133
	s_waitcnt vmcnt(18)
	v_cvt_f32_fp8_e32 v96, v32
	v_cvt_f32_fp8_sdwa v97, v32 src0_sel:BYTE_1
	v_cvt_f32_fp8_sdwa v98, v32 src0_sel:BYTE_2
	v_cvt_f32_fp8_sdwa v99, v32 src0_sel:BYTE_3
	v_cvt_f32_fp8_e32 v100, v33
	v_cvt_f32_fp8_sdwa v101, v33 src0_sel:BYTE_1
	v_cvt_f32_fp8_sdwa v102, v33 src0_sel:BYTE_2
	v_cvt_f32_fp8_sdwa v103, v33 src0_sel:BYTE_3
	v_pk_add_f32 v[64:65], v[64:65], v[96:97]
	v_pk_add_f32 v[66:67], v[66:67], v[98:99]
	v_pk_add_f32 v[68:69], v[68:69], v[100:101]
	v_pk_add_f32 v[70:71], v[70:71], v[102:103]
	v_cvt_f32_fp8_e32 v96, v40
	v_cvt_f32_fp8_sdwa v97, v40 src0_sel:BYTE_1
	v_cvt_f32_fp8_sdwa v98, v40 src0_sel:BYTE_2
	v_cvt_f32_fp8_sdwa v99, v40 src0_sel:BYTE_3
	v_cvt_f32_fp8_e32 v100, v41
	v_cvt_f32_fp8_sdwa v101, v41 src0_sel:BYTE_1
	v_cvt_f32_fp8_sdwa v102, v41 src0_sel:BYTE_2
	v_cvt_f32_fp8_sdwa v103, v41 src0_sel:BYTE_3
	v_pk_add_f32 v[64:65], v[64:65], v[96:97]
	v_pk_add_f32 v[66:67], v[66:67], v[98:99]
	v_pk_add_f32 v[68:69], v[68:69], v[100:101]
	v_pk_add_f32 v[70:71], v[70:71], v[102:103]
	v_cvt_f32_fp8_e32 v96, v48
	v_cvt_f32_fp8_sdwa v97, v48 src0_sel:BYTE_1
	v_cvt_f32_fp8_sdwa v98, v48 src0_sel:BYTE_2
	v_cvt_f32_fp8_sdwa v99, v48 src0_sel:BYTE_3
	v_cvt_f32_fp8_e32 v100, v49
	v_cvt_f32_fp8_sdwa v101, v49 src0_sel:BYTE_1
	v_cvt_f32_fp8_sdwa v102, v49 src0_sel:BYTE_2
	v_cvt_f32_fp8_sdwa v103, v49 src0_sel:BYTE_3
	v_pk_add_f32 v[64:65], v[64:65], v[96:97]
	v_pk_add_f32 v[66:67], v[66:67], v[98:99]
	v_pk_add_f32 v[68:69], v[68:69], v[100:101]
	v_pk_add_f32 v[70:71], v[70:71], v[102:103]
	v_cvt_f32_fp8_e32 v96, v56
	v_cvt_f32_fp8_sdwa v97, v56 src0_sel:BYTE_1
	v_cvt_f32_fp8_sdwa v98, v56 src0_sel:BYTE_2
	v_cvt_f32_fp8_sdwa v99, v56 src0_sel:BYTE_3
	v_cvt_f32_fp8_e32 v100, v57
	v_cvt_f32_fp8_sdwa v101, v57 src0_sel:BYTE_1
	v_cvt_f32_fp8_sdwa v102, v57 src0_sel:BYTE_2
	v_cvt_f32_fp8_sdwa v103, v57 src0_sel:BYTE_3
	v_pk_add_f32 v[64:65], v[64:65], v[96:97]
	v_pk_add_f32 v[66:67], v[66:67], v[98:99]
	v_pk_add_f32 v[68:69], v[68:69], v[100:101]
	v_pk_add_f32 v[70:71], v[70:71], v[102:103]
	s_waitcnt vmcnt(14)
; __device__ __forceinline__ void p12_final(const Frame& F, const KArgs& a) {
;     ...
;             for (int k = 0; k < 4; ++k) { const int y = *(const int*)(YB + so[k] + c);
;                 v[j][0] += __builtin_amdgcn_cvt_f32_fp8(y, 0); v[j][1] += __builtin_amdgcn_cvt_f32_fp8(y, 1); v[j][2] += __builtin_amdgcn_cvt_f32_fp8(y, 2); v[j][3] += __builtin_amdgcn_cvt_f32_fp8(y, 3); }
;             q += (v[j][0] * v[j][0] + v[j][1] * v[j][1]) + (v[j][2] * v[j][2] + v[j][3] * v[j][3]); }
	v_cvt_f32_fp8_e32 v96, v34
	v_cvt_f32_fp8_sdwa v97, v34 src0_sel:BYTE_1
	v_cvt_f32_fp8_sdwa v98, v34 src0_sel:BYTE_2
	v_cvt_f32_fp8_sdwa v99, v34 src0_sel:BYTE_3
	v_cvt_f32_fp8_e32 v100, v35
	v_cvt_f32_fp8_sdwa v101, v35 src0_sel:BYTE_1
	v_cvt_f32_fp8_sdwa v102, v35 src0_sel:BYTE_2
	v_cvt_f32_fp8_sdwa v103, v35 src0_sel:BYTE_3
	v_pk_add_f32 v[72:73], v[72:73], v[96:97]
	v_pk_add_f32 v[74:75], v[74:75], v[98:99]
	v_pk_add_f32 v[76:77], v[76:77], v[100:101]
	v_pk_add_f32 v[78:79], v[78:79], v[102:103]
	v_cvt_f32_fp8_e32 v96, v42
	v_cvt_f32_fp8_sdwa v97, v42 src0_sel:BYTE_1
	v_cvt_f32_fp8_sdwa v98, v42 src0_sel:BYTE_2
	v_cvt_f32_fp8_sdwa v99, v42 src0_sel:BYTE_3
	v_cvt_f32_fp8_e32 v100, v43
	v_cvt_f32_fp8_sdwa v101, v43 src0_sel:BYTE_1
	v_cvt_f32_fp8_sdwa v102, v43 src0_sel:BYTE_2
	v_cvt_f32_fp8_sdwa v103, v43 src0_sel:BYTE_3
	v_pk_add_f32 v[72:73], v[72:73], v[96:97]
	v_pk_add_f32 v[74:75], v[74:75], v[98:99]
	v_pk_add_f32 v[76:77], v[76:77], v[100:101]
	v_pk_add_f32 v[78:79], v[78:79], v[102:103]
	v_cvt_f32_fp8_e32 v96, v50
	v_cvt_f32_fp8_sdwa v97, v50 src0_sel:BYTE_1
	v_cvt_f32_fp8_sdwa v98, v50 src0_sel:BYTE_2
	v_cvt_f32_fp8_sdwa v99, v50 src0_sel:BYTE_3
	v_cvt_f32_fp8_e32 v100, v51
	v_cvt_f32_fp8_sdwa v101, v51 src0_sel:BYTE_1
	v_cvt_f32_fp8_sdwa v102, v51 src0_sel:BYTE_2
	v_cvt_f32_fp8_sdwa v103, v51 src0_sel:BYTE_3
	v_pk_add_f32 v[72:73], v[72:73], v[96:97]
	v_pk_add_f32 v[74:75], v[74:75], v[98:99]
	v_pk_add_f32 v[76:77], v[76:77], v[100:101]
	v_pk_add_f32 v[78:79], v[78:79], v[102:103]
	v_cvt_f32_fp8_e32 v96, v58
	v_cvt_f32_fp8_sdwa v97, v58 src0_sel:BYTE_1
	v_cvt_f32_fp8_sdwa v98, v58 src0_sel:BYTE_2
	v_cvt_f32_fp8_sdwa v99, v58 src0_sel:BYTE_3
	v_cvt_f32_fp8_e32 v100, v59
	v_cvt_f32_fp8_sdwa v101, v59 src0_sel:BYTE_1
	v_cvt_f32_fp8_sdwa v102, v59 src0_sel:BYTE_2
	v_cvt_f32_fp8_sdwa v103, v59 src0_sel:BYTE_3
	v_pk_add_f32 v[72:73], v[72:73], v[96:97]
	v_pk_add_f32 v[74:75], v[74:75], v[98:99]
	v_pk_add_f32 v[76:77], v[76:77], v[100:101]
	v_pk_add_f32 v[78:79], v[78:79], v[102:103]
	s_waitcnt vmcnt(10)
	v_cvt_f32_fp8_e32 v96, v36
	v_cvt_f32_fp8_sdwa v97, v36 src0_sel:BYTE_1
	v_cvt_f32_fp8_sdwa v98, v36 src0_sel:BYTE_2
	v_cvt_f32_fp8_sdwa v99, v36 src0_sel:BYTE_3
	v_cvt_f32_fp8_e32 v100, v37
	v_cvt_f32_fp8_sdwa v101, v37 src0_sel:BYTE_1
	v_cvt_f32_fp8_sdwa v102, v37 src0_sel:BYTE_2
	v_cvt_f32_fp8_sdwa v103, v37 src0_sel:BYTE_3
	v_pk_add_f32 v[80:81], v[80:81], v[96:97]
	v_pk_add_f32 v[82:83], v[82:83], v[98:99]
	v_pk_add_f32 v[84:85], v[84:85], v[100:101]
	v_pk_add_f32 v[86:87], v[86:87], v[102:103]
	v_cvt_f32_fp8_e32 v96, v44
	v_cvt_f32_fp8_sdwa v97, v44 src0_sel:BYTE_1
	v_cvt_f32_fp8_sdwa v98, v44 src0_sel:BYTE_2
	v_cvt_f32_fp8_sdwa v99, v44 src0_sel:BYTE_3
	v_cvt_f32_fp8_e32 v100, v45
	v_cvt_f32_fp8_sdwa v101, v45 src0_sel:BYTE_1
	v_cvt_f32_fp8_sdwa v102, v45 src0_sel:BYTE_2
	v_cvt_f32_fp8_sdwa v103, v45 src0_sel:BYTE_3
	v_pk_add_f32 v[80:81], v[80:81], v[96:97]
	v_pk_add_f32 v[82:83], v[82:83], v[98:99]
	v_pk_add_f32 v[84:85], v[84:85], v[100:101]
	v_pk_add_f32 v[86:87], v[86:87], v[102:103]
	v_cvt_f32_fp8_e32 v96, v52
	v_cvt_f32_fp8_sdwa v97, v52 src0_sel:BYTE_1
	v_cvt_f32_fp8_sdwa v98, v52 src0_sel:BYTE_2
	v_cvt_f32_fp8_sdwa v99, v52 src0_sel:BYTE_3
	v_cvt_f32_fp8_e32 v100, v53
	v_cvt_f32_fp8_sdwa v101, v53 src0_sel:BYTE_1
	v_cvt_f32_fp8_sdwa v102, v53 src0_sel:BYTE_2
	v_cvt_f32_fp8_sdwa v103, v53 src0_sel:BYTE_3
	v_pk_add_f32 v[80:81], v[80:81], v[96:97]
	v_pk_add_f32 v[82:83], v[82:83], v[98:99]
	v_pk_add_f32 v[84:85], v[84:85], v[100:101]
	v_pk_add_f32 v[86:87], v[86:87], v[102:103]
	v_cvt_f32_fp8_e32 v96, v60
	v_cvt_f32_fp8_sdwa v97, v60 src0_sel:BYTE_1
	v_cvt_f32_fp8_sdwa v98, v60 src0_sel:BYTE_2
	v_cvt_f32_fp8_sdwa v99, v60 src0_sel:BYTE_3
	v_cvt_f32_fp8_e32 v100, v61
	v_cvt_f32_fp8_sdwa v101, v61 src0_sel:BYTE_1
	v_cvt_f32_fp8_sdwa v102, v61 src0_sel:BYTE_2
	v_cvt_f32_fp8_sdwa v103, v61 src0_sel:BYTE_3
	v_pk_add_f32 v[80:81], v[80:81], v[96:97]
	v_pk_add_f32 v[82:83], v[82:83], v[98:99]
	v_pk_add_f32 v[84:85], v[84:85], v[100:101]
	v_pk_add_f32 v[86:87], v[86:87], v[102:103]
	s_waitcnt vmcnt(6)
; __device__ __forceinline__ void p12_final(const Frame& F, const KArgs& a) {
;     ...
;             for (int k = 0; k < 4; ++k) { const int y = *(const int*)(YB + so[k] + c);
;                 v[j][0] += __builtin_amdgcn_cvt_f32_fp8(y, 0); v[j][1] += __builtin_amdgcn_cvt_f32_fp8(y, 1); v[j][2] += __builtin_amdgcn_cvt_f32_fp8(y, 2); v[j][3] += __builtin_amdgcn_cvt_f32_fp8(y, 3); }
;             q += (v[j][0] * v[j][0] + v[j][1] * v[j][1]) + (v[j][2] * v[j][2] + v[j][3] * v[j][3]); }
;         const float rs = rsqrtf(wave_sum(q) * (1.f / DM) + RMS_EPS);
; #pragma unroll
;         for (int j = 0; j < 8; ++j) { const int c = 4 * (lane + 64 * j); const f32x4 g = *(const f32x4*)(a.in[24] + c); *(f32x4*)(a.out + (size_t)row * DM + c) = v[j] * rs * g; }
;     }
	v_cvt_f32_fp8_e32 v96, v38
	v_cvt_f32_fp8_sdwa v97, v38 src0_sel:BYTE_1
	v_cvt_f32_fp8_sdwa v98, v38 src0_sel:BYTE_2
	v_cvt_f32_fp8_sdwa v99, v38 src0_sel:BYTE_3
	v_cvt_f32_fp8_e32 v100, v39
	v_cvt_f32_fp8_sdwa v101, v39 src0_sel:BYTE_1
	v_cvt_f32_fp8_sdwa v102, v39 src0_sel:BYTE_2
	v_cvt_f32_fp8_sdwa v103, v39 src0_sel:BYTE_3
	v_pk_add_f32 v[88:89], v[88:89], v[96:97]
	v_pk_add_f32 v[90:91], v[90:91], v[98:99]
	v_pk_add_f32 v[92:93], v[92:93], v[100:101]
	v_pk_add_f32 v[94:95], v[94:95], v[102:103]
	v_cvt_f32_fp8_e32 v96, v46
	v_cvt_f32_fp8_sdwa v97, v46 src0_sel:BYTE_1
	v_cvt_f32_fp8_sdwa v98, v46 src0_sel:BYTE_2
	v_cvt_f32_fp8_sdwa v99, v46 src0_sel:BYTE_3
	v_cvt_f32_fp8_e32 v100, v47
	v_cvt_f32_fp8_sdwa v101, v47 src0_sel:BYTE_1
	v_cvt_f32_fp8_sdwa v102, v47 src0_sel:BYTE_2
	v_cvt_f32_fp8_sdwa v103, v47 src0_sel:BYTE_3
	v_pk_add_f32 v[88:89], v[88:89], v[96:97]
	v_pk_add_f32 v[90:91], v[90:91], v[98:99]
	v_pk_add_f32 v[92:93], v[92:93], v[100:101]
	v_pk_add_f32 v[94:95], v[94:95], v[102:103]
	v_cvt_f32_fp8_e32 v96, v54
	v_cvt_f32_fp8_sdwa v97, v54 src0_sel:BYTE_1
	v_cvt_f32_fp8_sdwa v98, v54 src0_sel:BYTE_2
	v_cvt_f32_fp8_sdwa v99, v54 src0_sel:BYTE_3
	v_cvt_f32_fp8_e32 v100, v55
	v_cvt_f32_fp8_sdwa v101, v55 src0_sel:BYTE_1
	v_cvt_f32_fp8_sdwa v102, v55 src0_sel:BYTE_2
	v_cvt_f32_fp8_sdwa v103, v55 src0_sel:BYTE_3
	v_pk_add_f32 v[88:89], v[88:89], v[96:97]
	v_pk_add_f32 v[90:91], v[90:91], v[98:99]
	v_pk_add_f32 v[92:93], v[92:93], v[100:101]
	v_pk_add_f32 v[94:95], v[94:95], v[102:103]
	v_cvt_f32_fp8_e32 v96, v62
	v_cvt_f32_fp8_sdwa v97, v62 src0_sel:BYTE_1
	v_cvt_f32_fp8_sdwa v98, v62 src0_sel:BYTE_2
	v_cvt_f32_fp8_sdwa v99, v62 src0_sel:BYTE_3
	v_cvt_f32_fp8_e32 v100, v63
	v_cvt_f32_fp8_sdwa v101, v63 src0_sel:BYTE_1
	v_cvt_f32_fp8_sdwa v102, v63 src0_sel:BYTE_2
	v_cvt_f32_fp8_sdwa v103, v63 src0_sel:BYTE_3
	v_pk_add_f32 v[88:89], v[88:89], v[96:97]
	v_pk_add_f32 v[90:91], v[90:91], v[98:99]
	v_pk_add_f32 v[92:93], v[92:93], v[100:101]
	v_pk_add_f32 v[94:95], v[94:95], v[102:103]
	v_pk_mul_f32 v[106:107], v[64:65], v[64:65]
	v_pk_fma_f32 v[106:107], v[66:67], v[66:67], v[106:107]
	v_pk_fma_f32 v[106:107], v[68:69], v[68:69], v[106:107]
	v_pk_fma_f32 v[106:107], v[70:71], v[70:71], v[106:107]
	v_pk_fma_f32 v[106:107], v[72:73], v[72:73], v[106:107]
	v_pk_fma_f32 v[106:107], v[74:75], v[74:75], v[106:107]
	v_pk_fma_f32 v[106:107], v[76:77], v[76:77], v[106:107]
	v_pk_fma_f32 v[106:107], v[78:79], v[78:79], v[106:107]
	v_pk_fma_f32 v[106:107], v[80:81], v[80:81], v[106:107]
	v_pk_fma_f32 v[106:107], v[82:83], v[82:83], v[106:107]
	v_pk_fma_f32 v[106:107], v[84:85], v[84:85], v[106:107]
	v_pk_fma_f32 v[106:107], v[86:87], v[86:87], v[106:107]
	v_pk_fma_f32 v[106:107], v[88:89], v[88:89], v[106:107]
	v_pk_fma_f32 v[106:107], v[90:91], v[90:91], v[106:107]
	v_pk_fma_f32 v[106:107], v[92:93], v[92:93], v[106:107]
	v_pk_fma_f32 v[106:107], v[94:95], v[94:95], v[106:107]
	s_nop 0
	v_add_f32_e32 v105, v106, v107
	s_nop 1
	v_add_f32_dpp v105, v105, v105 quad_perm:[1,0,3,2] row_mask:0xf bank_mask:0xf
	s_nop 1
	v_add_f32_dpp v105, v105, v105 quad_perm:[2,3,0,1] row_mask:0xf bank_mask:0xf
	s_nop 1
	v_add_f32_dpp v105, v105, v105 row_half_mirror row_mask:0xf bank_mask:0xf
	s_nop 1
	v_add_f32_dpp v105, v105, v105 row_mirror row_mask:0xf bank_mask:0xf
	s_nop 1
	v_readlane_b32 s12, v105, 0
	v_readlane_b32 s14, v105, 16
	v_readlane_b32 s15, v105, 32
	v_readlane_b32 s16, v105, 48
	s_nop 1
	v_mov_b32_e32 v105, s12
	v_add_f32_e32 v105, s14, v105
	v_add_f32_e32 v105, s15, v105
	v_add_f32_e32 v105, s16, v105
	v_fmamk_f32 v105, v105, 0x3a000000, v104
	v_rsq_f32_e32 v108, v105
	s_nop 0
	v_pk_mul_f32 v[64:65], v[64:65], v[108:109] op_sel_hi:[1,0]
	v_pk_mul_f32 v[66:67], v[66:67], v[108:109] op_sel_hi:[1,0]
	v_pk_mul_f32 v[68:69], v[68:69], v[108:109] op_sel_hi:[1,0]
	v_pk_mul_f32 v[70:71], v[70:71], v[108:109] op_sel_hi:[1,0]
	v_pk_mul_f32 v[64:65], v[64:65], v[200:201]
	v_pk_mul_f32 v[66:67], v[66:67], v[202:203]
	v_pk_mul_f32 v[68:69], v[68:69], v[204:205]
	v_pk_mul_f32 v[70:71], v[70:71], v[206:207]
	global_store_dwordx4 v4, v[64:67], s[18:19] nt
	global_store_dwordx4 v4, v[68:71], s[18:19] offset:16 nt
	v_pk_mul_f32 v[72:73], v[72:73], v[108:109] op_sel_hi:[1,0]
	v_pk_mul_f32 v[74:75], v[74:75], v[108:109] op_sel_hi:[1,0]
	v_pk_mul_f32 v[76:77], v[76:77], v[108:109] op_sel_hi:[1,0]
	v_pk_mul_f32 v[78:79], v[78:79], v[108:109] op_sel_hi:[1,0]
	v_pk_mul_f32 v[72:73], v[72:73], v[208:209]
	v_pk_mul_f32 v[74:75], v[74:75], v[210:211]
	v_pk_mul_f32 v[76:77], v[76:77], v[212:213]
	v_pk_mul_f32 v[78:79], v[78:79], v[214:215]
	global_store_dwordx4 v4, v[72:75], s[18:19] offset:2048 nt
	global_store_dwordx4 v4, v[76:79], s[18:19] offset:2064 nt
	v_pk_mul_f32 v[80:81], v[80:81], v[108:109] op_sel_hi:[1,0]
	v_pk_mul_f32 v[82:83], v[82:83], v[108:109] op_sel_hi:[1,0]
	v_pk_mul_f32 v[84:85], v[84:85], v[108:109] op_sel_hi:[1,0]
	v_pk_mul_f32 v[86:87], v[86:87], v[108:109] op_sel_hi:[1,0]
	v_pk_mul_f32 v[80:81], v[80:81], v[216:217]
	v_pk_mul_f32 v[82:83], v[82:83], v[218:219]
	v_pk_mul_f32 v[84:85], v[84:85], v[220:221]
	v_pk_mul_f32 v[86:87], v[86:87], v[222:223]
	global_store_dwordx4 v4, v[80:83], s[24:25] nt
	global_store_dwordx4 v4, v[84:87], s[24:25] offset:16 nt
	v_pk_mul_f32 v[88:89], v[88:89], v[108:109] op_sel_hi:[1,0]
	v_pk_mul_f32 v[90:91], v[90:91], v[108:109] op_sel_hi:[1,0]
	v_pk_mul_f32 v[92:93], v[92:93], v[108:109] op_sel_hi:[1,0]
	v_pk_mul_f32 v[94:95], v[94:95], v[108:109] op_sel_hi:[1,0]
	v_pk_mul_f32 v[88:89], v[88:89], v[224:225]
	v_pk_mul_f32 v[90:91], v[90:91], v[226:227]
	v_pk_mul_f32 v[92:93], v[92:93], v[228:229]
	v_pk_mul_f32 v[94:95], v[94:95], v[230:231]
	global_store_dwordx4 v4, v[88:91], s[24:25] offset:2048 nt
	global_store_dwordx4 v4, v[92:95], s[24:25] offset:2064 nt
	s_mov_b32 s20, s21
	s_cmpk_lt_i32 s20, 0x4000
	s_cbranch_scc1 .Lp12_row
